# NSA in-proj epilogue: rotary cos/sin table loads of row group g+1 prefetched into dead fragment VGPRs while group g is rotated/stored (8 serialized load latencies -> 1)
# baseline (speedup 1.0000x reference)
.LBB0_172:
	s_and_b64 s[40:41], s[22:23], s[40:41]
	v_cndmask_b32_e64 v90, 0, 1, s[40:41]
	v_cmp_ne_u32_e64 s[14:15], 1, v90
	s_andn2_b64 vcc, exec, s[40:41]
	v_and_b32_e32 v201, 0xfcf, v200
	s_cbranch_vccnz .LBB0_174
	v_lshlrev_b32_e32 v162, 6, v201
	v_lshl_add_u64 v[102:103], v[166:167], 0, v[162:163]
	v_lshl_add_u64 v[94:95], v[168:169], 0, v[162:163]
	v_mov_b64_e32 v[202:203], v[94:95]
	v_mov_b64_e32 v[204:205], v[102:103]
	v_add_co_u32_e32 v222, vcc, 0x2000, v94
	s_nop 1
	v_addc_co_u32_e32 v223, vcc, 0, v95, vcc
	v_add_co_u32_e32 v224, vcc, 0x2000, v102
	s_nop 1
	v_addc_co_u32_e32 v225, vcc, 0, v103, vcc
	global_load_dwordx4 v[90:93], v[94:95], off offset:16
	s_nop 0
	global_load_dwordx4 v[94:97], v[94:95], off
	s_nop 0
	global_load_dwordx4 v[98:101], v[102:103], off offset:16
	s_nop 0
	global_load_dwordx4 v[102:105], v[102:103], off
	global_load_dwordx4 v[206:209], v[202:203], off offset:1040
	global_load_dwordx4 v[210:213], v[202:203], off offset:1024
	global_load_dwordx4 v[214:217], v[204:205], off offset:1040
	global_load_dwordx4 v[218:221], v[204:205], off offset:1024
.LBB0_174:
	v_mov_b64_e32 v[148:149], v[72:73]
	v_mov_b64_e32 v[152:153], v[68:69]
	s_and_b64 vcc, exec, s[14:15]
	v_mov_b64_e32 v[146:147], v[70:71]
	v_mov_b64_e32 v[150:151], v[66:67]
	s_cbranch_vccnz .LBB0_180
	v_mov_b32_e32 v146, v70
	v_mov_b32_e32 v147, v70
	s_nop 1
	v_permlane32_swap_b32_e32 v146, v147
	v_cndmask_b32_e64 v146, v146, v147, s[8:9]
	v_mov_b32_e32 v147, v66
	v_mov_b32_e32 v148, v66
	s_nop 1
	v_permlane32_swap_b32_e32 v147, v148
	v_cndmask_b32_e64 v148, v147, v148, s[8:9]
	v_mov_b32_e32 v147, v71
	v_mov_b32_e32 v149, v71
	s_nop 1
	v_permlane32_swap_b32_e32 v147, v149
	v_cndmask_b32_e64 v147, v147, v149, s[8:9]
	v_mov_b32_e32 v149, v67
	v_mov_b32_e32 v150, v67
	s_nop 1
	v_permlane32_swap_b32_e32 v149, v150
	v_cndmask_b32_e64 v149, v149, v150, s[8:9]
	v_mov_b32_e32 v150, v72
	v_mov_b32_e32 v151, v72
	s_nop 1
	v_permlane32_swap_b32_e32 v150, v151
	v_cndmask_b32_e64 v150, v150, v151, s[8:9]
	v_mov_b32_e32 v151, v68
	v_mov_b32_e32 v152, v68
	s_nop 1
	v_permlane32_swap_b32_e32 v151, v152
	v_cndmask_b32_e64 v152, v151, v152, s[8:9]
	v_mov_b32_e32 v151, v73
	v_mov_b32_e32 v153, v73
	s_nop 1
	v_permlane32_swap_b32_e32 v151, v153
	v_cndmask_b32_e64 v151, v151, v153, s[8:9]
	v_mov_b32_e32 v153, v69
	v_mov_b32_e32 v162, v69
	s_nop 1
	v_permlane32_swap_b32_e32 v153, v162
	v_cndmask_b32_e64 v153, v153, v162, s[8:9]
	s_waitcnt vmcnt(4)
	v_pk_mul_f32 v[180:181], v[72:73], v[96:97]
	v_pk_mul_f32 v[182:183], v[70:71], v[94:95]
	v_pk_mul_f32 v[188:189], v[104:105], v[150:151]
	v_pk_mul_f32 v[192:193], v[102:103], v[146:147]
	v_pk_mul_f32 v[184:185], v[68:69], v[92:93]
	v_pk_mul_f32 v[186:187], v[66:67], v[90:91]
	v_pk_mul_f32 v[190:191], v[100:101], v[152:153]
	v_pk_mul_f32 v[194:195], v[98:99], v[148:149]
	s_and_saveexec_b64 s[40:41], s[10:11]
	s_xor_b64 s[40:41], exec, s[40:41]
	v_pk_add_f32 v[148:149], v[180:181], v[188:189]
	v_pk_add_f32 v[146:147], v[182:183], v[192:193]
	v_pk_add_f32 v[152:153], v[184:185], v[190:191]
	v_pk_add_f32 v[150:151], v[186:187], v[194:195]
	s_andn2_saveexec_b64 s[40:41], s[40:41]
	v_sub_f32_e32 v149, v181, v189
	v_sub_f32_e32 v148, v180, v188
	v_sub_f32_e32 v147, v183, v193
	v_sub_f32_e32 v146, v182, v192
	v_sub_f32_e32 v153, v185, v191
	v_sub_f32_e32 v152, v184, v190
	v_sub_f32_e32 v151, v187, v195
	v_sub_f32_e32 v150, v186, v194
	s_or_b64 exec, exec, s[40:41]

.LBB0_194:
	v_cvt_pk_bf16_f32 v142, v142, v143
	v_cvt_pk_bf16_f32 v143, v144, v145
	v_cvt_pk_bf16_f32 v144, v138, v139
	v_lshl_add_u64 v[138:139], v[148:149], 1, s[36:37]
	s_and_b64 vcc, exec, s[14:15]
	v_bitop3_b32 v192, v200, s59, 16 bitop3:0xc8
	v_cvt_pk_bf16_f32 v145, v140, v141
	global_store_dwordx4 v[138:139], v[142:145], off
	s_cbranch_vccnz .LBB0_196
	s_waitcnt vmcnt(2)
	v_mov_b64_e32 v[90:91], v[206:207]
	v_mov_b64_e32 v[92:93], v[208:209]
	v_mov_b64_e32 v[94:95], v[210:211]
	v_mov_b64_e32 v[96:97], v[212:213]
	v_mov_b64_e32 v[98:99], v[214:215]
	v_mov_b64_e32 v[100:101], v[216:217]
	v_mov_b64_e32 v[102:103], v[218:219]
	v_mov_b64_e32 v[104:105], v[220:221]
	global_load_dwordx4 v[206:209], v[202:203], off offset:2064
	global_load_dwordx4 v[210:213], v[202:203], off offset:2048
	global_load_dwordx4 v[214:217], v[204:205], off offset:2064
	global_load_dwordx4 v[218:221], v[204:205], off offset:2048
.LBB0_196:
	v_mov_b64_e32 v[140:141], v[56:57]
	v_mov_b64_e32 v[144:145], v[52:53]
	s_and_b64 vcc, exec, s[14:15]
	v_mov_b64_e32 v[138:139], v[54:55]
	v_mov_b64_e32 v[142:143], v[50:51]
	s_cbranch_vccnz .LBB0_202
	v_mov_b32_e32 v138, v54
	v_mov_b32_e32 v139, v54
	s_nop 1
	v_permlane32_swap_b32_e32 v138, v139
	v_cndmask_b32_e64 v138, v138, v139, s[8:9]
	v_mov_b32_e32 v139, v50
	v_mov_b32_e32 v140, v50
	s_nop 1
	v_permlane32_swap_b32_e32 v139, v140
	v_cndmask_b32_e64 v140, v139, v140, s[8:9]
	v_mov_b32_e32 v139, v55
	v_mov_b32_e32 v141, v55
	s_nop 1
	v_permlane32_swap_b32_e32 v139, v141
	v_cndmask_b32_e64 v139, v139, v141, s[8:9]
	v_mov_b32_e32 v141, v51
	v_mov_b32_e32 v142, v51
	s_nop 1
	v_permlane32_swap_b32_e32 v141, v142
	v_cndmask_b32_e64 v141, v141, v142, s[8:9]
	v_mov_b32_e32 v142, v56
	v_mov_b32_e32 v143, v56
	s_nop 1
	v_permlane32_swap_b32_e32 v142, v143
	v_cndmask_b32_e64 v142, v142, v143, s[8:9]
	v_mov_b32_e32 v143, v52
	v_mov_b32_e32 v144, v52
	s_nop 1
	v_permlane32_swap_b32_e32 v143, v144
	v_cndmask_b32_e64 v144, v143, v144, s[8:9]
	v_mov_b32_e32 v143, v57
	v_mov_b32_e32 v145, v57
	s_nop 1
	v_permlane32_swap_b32_e32 v143, v145
	v_cndmask_b32_e64 v143, v143, v145, s[8:9]
	v_mov_b32_e32 v145, v53
	v_mov_b32_e32 v148, v53
	s_nop 1
	v_permlane32_swap_b32_e32 v145, v148
	v_cndmask_b32_e64 v145, v145, v148, s[8:9]
	v_pk_mul_f32 v[148:149], v[56:57], v[96:97]
	v_pk_mul_f32 v[150:151], v[54:55], v[94:95]
	v_pk_mul_f32 v[184:185], v[104:105], v[142:143]
	v_pk_mul_f32 v[188:189], v[102:103], v[138:139]
	v_pk_mul_f32 v[152:153], v[52:53], v[92:93]
	v_pk_mul_f32 v[182:183], v[50:51], v[90:91]
	v_pk_mul_f32 v[186:187], v[100:101], v[144:145]
	v_pk_mul_f32 v[190:191], v[98:99], v[140:141]
	s_and_saveexec_b64 s[40:41], s[10:11]
	s_xor_b64 s[40:41], exec, s[40:41]
	v_pk_add_f32 v[140:141], v[148:149], v[184:185]
	v_pk_add_f32 v[138:139], v[150:151], v[188:189]
	v_pk_add_f32 v[144:145], v[152:153], v[186:187]
	v_pk_add_f32 v[142:143], v[182:183], v[190:191]
	s_andn2_saveexec_b64 s[40:41], s[40:41]
	v_sub_f32_e32 v141, v149, v185
	v_sub_f32_e32 v140, v148, v184
	v_sub_f32_e32 v139, v151, v189
	v_sub_f32_e32 v138, v150, v188
	v_sub_f32_e32 v145, v153, v187
	v_sub_f32_e32 v144, v152, v186
	v_sub_f32_e32 v143, v183, v191
	v_sub_f32_e32 v142, v182, v190
	s_or_b64 exec, exec, s[40:41]

.LBB0_210:
	v_cvt_pk_bf16_f32 v134, v134, v135
	v_cvt_pk_bf16_f32 v135, v136, v137
	v_cvt_pk_bf16_f32 v136, v130, v131
	v_lshl_add_u64 v[130:131], v[138:139], 1, s[36:37]
	s_and_b64 vcc, exec, s[14:15]
	v_bitop3_b32 v184, v200, s60, 32 bitop3:0xc8
	v_cvt_pk_bf16_f32 v137, v132, v133
	global_store_dwordx4 v[130:131], v[134:137], off
	s_cbranch_vccnz .LBB0_212
	s_waitcnt vmcnt(2)
	v_mov_b64_e32 v[90:91], v[206:207]
	v_mov_b64_e32 v[92:93], v[208:209]
	v_mov_b64_e32 v[94:95], v[210:211]
	v_mov_b64_e32 v[96:97], v[212:213]
	v_mov_b64_e32 v[98:99], v[214:215]
	v_mov_b64_e32 v[100:101], v[216:217]
	v_mov_b64_e32 v[102:103], v[218:219]
	v_mov_b64_e32 v[104:105], v[220:221]
	global_load_dwordx4 v[206:209], v[202:203], off offset:3088
	global_load_dwordx4 v[210:213], v[202:203], off offset:3072
	global_load_dwordx4 v[214:217], v[204:205], off offset:3088
	global_load_dwordx4 v[218:221], v[204:205], off offset:3072
.LBB0_212:
	v_mov_b64_e32 v[132:133], v[48:49]
	v_mov_b64_e32 v[136:137], v[44:45]
	s_and_b64 vcc, exec, s[14:15]
	v_mov_b64_e32 v[130:131], v[46:47]
	v_mov_b64_e32 v[134:135], v[42:43]
	s_cbranch_vccnz .LBB0_218
	v_mov_b32_e32 v130, v46
	v_mov_b32_e32 v131, v46
	s_nop 1
	v_permlane32_swap_b32_e32 v130, v131
	v_cndmask_b32_e64 v130, v130, v131, s[8:9]
	v_mov_b32_e32 v131, v42
	v_mov_b32_e32 v132, v42
	s_nop 1
	v_permlane32_swap_b32_e32 v131, v132
	v_cndmask_b32_e64 v132, v131, v132, s[8:9]
	v_mov_b32_e32 v131, v47
	v_mov_b32_e32 v133, v47
	s_nop 1
	v_permlane32_swap_b32_e32 v131, v133
	v_cndmask_b32_e64 v131, v131, v133, s[8:9]
	v_mov_b32_e32 v133, v43
	v_mov_b32_e32 v134, v43
	s_nop 1
	v_permlane32_swap_b32_e32 v133, v134
	v_cndmask_b32_e64 v133, v133, v134, s[8:9]
	v_mov_b32_e32 v134, v48
	v_mov_b32_e32 v135, v48
	s_nop 1
	v_permlane32_swap_b32_e32 v134, v135
	v_cndmask_b32_e64 v134, v134, v135, s[8:9]
	v_mov_b32_e32 v135, v44
	v_mov_b32_e32 v136, v44
	s_nop 1
	v_permlane32_swap_b32_e32 v135, v136
	v_cndmask_b32_e64 v136, v135, v136, s[8:9]
	v_mov_b32_e32 v135, v49
	v_mov_b32_e32 v137, v49
	s_nop 1
	v_permlane32_swap_b32_e32 v135, v137
	v_cndmask_b32_e64 v135, v135, v137, s[8:9]
	v_mov_b32_e32 v137, v45
	v_mov_b32_e32 v138, v45
	s_nop 1
	v_permlane32_swap_b32_e32 v137, v138
	v_cndmask_b32_e64 v137, v137, v138, s[8:9]
	v_pk_mul_f32 v[138:139], v[48:49], v[96:97]
	v_pk_mul_f32 v[140:141], v[46:47], v[94:95]
	v_pk_mul_f32 v[148:149], v[104:105], v[134:135]
	v_pk_mul_f32 v[152:153], v[102:103], v[130:131]
	v_pk_mul_f32 v[142:143], v[44:45], v[92:93]
	v_pk_mul_f32 v[144:145], v[42:43], v[90:91]
	v_pk_mul_f32 v[150:151], v[100:101], v[136:137]
	v_pk_mul_f32 v[182:183], v[98:99], v[132:133]
	s_and_saveexec_b64 s[40:41], s[10:11]
	s_xor_b64 s[40:41], exec, s[40:41]
	v_pk_add_f32 v[132:133], v[138:139], v[148:149]
	v_pk_add_f32 v[130:131], v[140:141], v[152:153]
	v_pk_add_f32 v[136:137], v[142:143], v[150:151]
	v_pk_add_f32 v[134:135], v[144:145], v[182:183]
	s_andn2_saveexec_b64 s[40:41], s[40:41]
	v_sub_f32_e32 v133, v139, v149
	v_sub_f32_e32 v132, v138, v148
	v_sub_f32_e32 v131, v141, v153
	v_sub_f32_e32 v130, v140, v152
	v_sub_f32_e32 v137, v143, v151
	v_sub_f32_e32 v136, v142, v150
	v_sub_f32_e32 v135, v145, v183
	v_sub_f32_e32 v134, v144, v182
	s_or_b64 exec, exec, s[40:41]

.LBB0_226:
	v_cvt_pk_bf16_f32 v126, v126, v127
	v_cvt_pk_bf16_f32 v127, v128, v129
	v_cvt_pk_bf16_f32 v128, v122, v123
	v_lshl_add_u64 v[122:123], v[130:131], 1, s[36:37]
	s_and_b64 vcc, exec, s[14:15]
	v_bitop3_b32 v148, v200, s61, 48 bitop3:0xc8
	v_cvt_pk_bf16_f32 v129, v124, v125
	global_store_dwordx4 v[122:123], v[126:129], off
	s_cbranch_vccnz .LBB0_228
	s_waitcnt vmcnt(2)
	v_mov_b64_e32 v[90:91], v[206:207]
	v_mov_b64_e32 v[92:93], v[208:209]
	v_mov_b64_e32 v[94:95], v[210:211]
	v_mov_b64_e32 v[96:97], v[212:213]
	v_mov_b64_e32 v[98:99], v[214:215]
	v_mov_b64_e32 v[100:101], v[216:217]
	v_mov_b64_e32 v[102:103], v[218:219]
	v_mov_b64_e32 v[104:105], v[220:221]
	global_load_dwordx4 v[206:209], v[222:223], off offset:16
	global_load_dwordx4 v[210:213], v[222:223], off
	global_load_dwordx4 v[214:217], v[224:225], off offset:16
	global_load_dwordx4 v[218:221], v[224:225], off
.LBB0_228:
	v_mov_b64_e32 v[124:125], v[40:41]
	v_mov_b64_e32 v[128:129], v[36:37]
	s_and_b64 vcc, exec, s[14:15]
	v_mov_b64_e32 v[122:123], v[38:39]
	v_mov_b64_e32 v[126:127], v[34:35]
	s_cbranch_vccnz .LBB0_234
	v_mov_b32_e32 v122, v38
	v_mov_b32_e32 v123, v38
	s_nop 1
	v_permlane32_swap_b32_e32 v122, v123
	v_cndmask_b32_e64 v122, v122, v123, s[8:9]
	v_mov_b32_e32 v123, v34
	v_mov_b32_e32 v124, v34
	s_nop 1
	v_permlane32_swap_b32_e32 v123, v124
	v_cndmask_b32_e64 v124, v123, v124, s[8:9]
	v_mov_b32_e32 v123, v39
	v_mov_b32_e32 v125, v39
	s_nop 1
	v_permlane32_swap_b32_e32 v123, v125
	v_cndmask_b32_e64 v123, v123, v125, s[8:9]
	v_mov_b32_e32 v125, v35
	v_mov_b32_e32 v126, v35
	s_nop 1
	v_permlane32_swap_b32_e32 v125, v126
	v_cndmask_b32_e64 v125, v125, v126, s[8:9]
	v_mov_b32_e32 v126, v40
	v_mov_b32_e32 v127, v40
	s_nop 1
	v_permlane32_swap_b32_e32 v126, v127
	v_cndmask_b32_e64 v126, v126, v127, s[8:9]
	v_mov_b32_e32 v127, v36
	v_mov_b32_e32 v128, v36
	s_nop 1
	v_permlane32_swap_b32_e32 v127, v128
	v_cndmask_b32_e64 v128, v127, v128, s[8:9]
	v_mov_b32_e32 v127, v41
	v_mov_b32_e32 v129, v41
	s_nop 1
	v_permlane32_swap_b32_e32 v127, v129
	v_cndmask_b32_e64 v127, v127, v129, s[8:9]
	v_mov_b32_e32 v129, v37
	v_mov_b32_e32 v130, v37
	s_nop 1
	v_permlane32_swap_b32_e32 v129, v130
	v_cndmask_b32_e64 v129, v129, v130, s[8:9]
	v_pk_mul_f32 v[130:131], v[40:41], v[96:97]
	v_pk_mul_f32 v[132:133], v[38:39], v[94:95]
	v_pk_mul_f32 v[138:139], v[104:105], v[126:127]
	v_pk_mul_f32 v[142:143], v[102:103], v[122:123]
	v_pk_mul_f32 v[134:135], v[36:37], v[92:93]
	v_pk_mul_f32 v[136:137], v[34:35], v[90:91]
	v_pk_mul_f32 v[140:141], v[100:101], v[128:129]
	v_pk_mul_f32 v[144:145], v[98:99], v[124:125]
	s_and_saveexec_b64 s[40:41], s[10:11]
	s_xor_b64 s[40:41], exec, s[40:41]
	v_pk_add_f32 v[124:125], v[130:131], v[138:139]
	v_pk_add_f32 v[122:123], v[132:133], v[142:143]
	v_pk_add_f32 v[128:129], v[134:135], v[140:141]
	v_pk_add_f32 v[126:127], v[136:137], v[144:145]
	s_andn2_saveexec_b64 s[40:41], s[40:41]
	v_sub_f32_e32 v125, v131, v139
	v_sub_f32_e32 v124, v130, v138
	v_sub_f32_e32 v123, v133, v143
	v_sub_f32_e32 v122, v132, v142
	v_sub_f32_e32 v129, v135, v141
	v_sub_f32_e32 v128, v134, v140
	v_sub_f32_e32 v127, v137, v145
	v_sub_f32_e32 v126, v136, v144
	s_or_b64 exec, exec, s[40:41]

.LBB0_242:
	v_add_u32_e32 v138, 0x80, v200
	v_cvt_pk_bf16_f32 v118, v118, v119
	v_cvt_pk_bf16_f32 v119, v120, v121
	v_cvt_pk_bf16_f32 v120, v114, v115
	v_lshl_add_u64 v[114:115], v[122:123], 1, s[36:37]
	s_and_b64 vcc, exec, s[14:15]
	v_and_b32_e32 v139, 0xfcf, v138
	v_cvt_pk_bf16_f32 v121, v116, v117
	global_store_dwordx4 v[114:115], v[118:121], off
	s_cbranch_vccnz .LBB0_244
	s_waitcnt vmcnt(2)
	v_mov_b64_e32 v[90:91], v[206:207]
	v_mov_b64_e32 v[92:93], v[208:209]
	v_mov_b64_e32 v[94:95], v[210:211]
	v_mov_b64_e32 v[96:97], v[212:213]
	v_mov_b64_e32 v[98:99], v[214:215]
	v_mov_b64_e32 v[100:101], v[216:217]
	v_mov_b64_e32 v[102:103], v[218:219]
	v_mov_b64_e32 v[104:105], v[220:221]
	global_load_dwordx4 v[206:209], v[222:223], off offset:1040
	global_load_dwordx4 v[210:213], v[222:223], off offset:1024
	global_load_dwordx4 v[214:217], v[224:225], off offset:1040
	global_load_dwordx4 v[218:221], v[224:225], off offset:1024
.LBB0_244:
	v_mov_b64_e32 v[116:117], v[32:33]
	v_mov_b64_e32 v[120:121], v[28:29]
	s_and_b64 vcc, exec, s[14:15]
	v_mov_b64_e32 v[114:115], v[30:31]
	v_mov_b64_e32 v[118:119], v[26:27]
	s_cbranch_vccnz .LBB0_250
	v_mov_b32_e32 v114, v30
	v_mov_b32_e32 v115, v30
	s_nop 1
	v_permlane32_swap_b32_e32 v114, v115
	v_cndmask_b32_e64 v114, v114, v115, s[8:9]
	v_mov_b32_e32 v115, v26
	v_mov_b32_e32 v116, v26
	s_nop 1
	v_permlane32_swap_b32_e32 v115, v116
	v_cndmask_b32_e64 v116, v115, v116, s[8:9]
	v_mov_b32_e32 v115, v31
	v_mov_b32_e32 v117, v31
	s_nop 1
	v_permlane32_swap_b32_e32 v115, v117
	v_cndmask_b32_e64 v115, v115, v117, s[8:9]
	v_mov_b32_e32 v117, v27
	v_mov_b32_e32 v118, v27
	s_nop 1
	v_permlane32_swap_b32_e32 v117, v118
	v_cndmask_b32_e64 v117, v117, v118, s[8:9]
	v_mov_b32_e32 v118, v32
	v_mov_b32_e32 v119, v32
	s_nop 1
	v_permlane32_swap_b32_e32 v118, v119
	v_cndmask_b32_e64 v118, v118, v119, s[8:9]
	v_mov_b32_e32 v119, v28
	v_mov_b32_e32 v120, v28
	s_nop 1
	v_permlane32_swap_b32_e32 v119, v120
	v_cndmask_b32_e64 v120, v119, v120, s[8:9]
	v_mov_b32_e32 v119, v33
	v_mov_b32_e32 v121, v33
	s_nop 1
	v_permlane32_swap_b32_e32 v119, v121
	v_cndmask_b32_e64 v119, v119, v121, s[8:9]
	v_mov_b32_e32 v121, v29
	v_mov_b32_e32 v122, v29
	s_nop 1
	v_permlane32_swap_b32_e32 v121, v122
	v_cndmask_b32_e64 v121, v121, v122, s[8:9]
	v_pk_mul_f32 v[122:123], v[32:33], v[96:97]
	v_pk_mul_f32 v[124:125], v[30:31], v[94:95]
	v_pk_mul_f32 v[130:131], v[104:105], v[118:119]
	v_pk_mul_f32 v[134:135], v[102:103], v[114:115]
	v_pk_mul_f32 v[126:127], v[28:29], v[92:93]
	v_pk_mul_f32 v[128:129], v[26:27], v[90:91]
	v_pk_mul_f32 v[132:133], v[100:101], v[120:121]
	v_pk_mul_f32 v[136:137], v[98:99], v[116:117]
	s_and_saveexec_b64 s[40:41], s[10:11]
	s_xor_b64 s[40:41], exec, s[40:41]
	v_pk_add_f32 v[116:117], v[122:123], v[130:131]
	v_pk_add_f32 v[114:115], v[124:125], v[134:135]
	v_pk_add_f32 v[120:121], v[126:127], v[132:133]
	v_pk_add_f32 v[118:119], v[128:129], v[136:137]
	s_andn2_saveexec_b64 s[40:41], s[40:41]
	v_sub_f32_e32 v117, v123, v131
	v_sub_f32_e32 v116, v122, v130
	v_sub_f32_e32 v115, v125, v135
	v_sub_f32_e32 v114, v124, v134
	v_sub_f32_e32 v121, v127, v133
	v_sub_f32_e32 v120, v126, v132
	v_sub_f32_e32 v119, v129, v137
	v_sub_f32_e32 v118, v128, v136
	s_or_b64 exec, exec, s[40:41]

.LBB0_258:
	v_add_u32_e32 v131, 0x90, v200
	v_cvt_pk_bf16_f32 v110, v110, v111
	v_cvt_pk_bf16_f32 v111, v112, v113
	v_cvt_pk_bf16_f32 v112, v106, v107
	v_lshl_add_u64 v[106:107], v[114:115], 1, s[36:37]
	s_and_b64 vcc, exec, s[14:15]
	v_and_b32_e32 v130, 0xfdf, v131
	v_cvt_pk_bf16_f32 v113, v108, v109
	global_store_dwordx4 v[106:107], v[110:113], off
	s_cbranch_vccnz .LBB0_260
	s_waitcnt vmcnt(2)
	v_mov_b64_e32 v[90:91], v[206:207]
	v_mov_b64_e32 v[92:93], v[208:209]
	v_mov_b64_e32 v[94:95], v[210:211]
	v_mov_b64_e32 v[96:97], v[212:213]
	v_mov_b64_e32 v[98:99], v[214:215]
	v_mov_b64_e32 v[100:101], v[216:217]
	v_mov_b64_e32 v[102:103], v[218:219]
	v_mov_b64_e32 v[104:105], v[220:221]
	global_load_dwordx4 v[206:209], v[222:223], off offset:2064
	global_load_dwordx4 v[210:213], v[222:223], off offset:2048
	global_load_dwordx4 v[214:217], v[224:225], off offset:2064
	global_load_dwordx4 v[218:221], v[224:225], off offset:2048
.LBB0_260:
	v_mov_b64_e32 v[108:109], v[24:25]
	v_mov_b64_e32 v[112:113], v[20:21]
	s_and_b64 vcc, exec, s[14:15]
	v_mov_b64_e32 v[106:107], v[22:23]
	v_mov_b64_e32 v[110:111], v[18:19]
	s_cbranch_vccnz .LBB0_266
	v_mov_b32_e32 v106, v22
	v_mov_b32_e32 v107, v22
	s_nop 1
	v_permlane32_swap_b32_e32 v106, v107
	v_cndmask_b32_e64 v106, v106, v107, s[8:9]
	v_mov_b32_e32 v107, v18
	v_mov_b32_e32 v108, v18
	s_nop 1
	v_permlane32_swap_b32_e32 v107, v108
	v_cndmask_b32_e64 v108, v107, v108, s[8:9]
	v_mov_b32_e32 v107, v23
	v_mov_b32_e32 v109, v23
	s_nop 1
	v_permlane32_swap_b32_e32 v107, v109
	v_cndmask_b32_e64 v107, v107, v109, s[8:9]
	v_mov_b32_e32 v109, v19
	v_mov_b32_e32 v110, v19
	s_nop 1
	v_permlane32_swap_b32_e32 v109, v110
	v_cndmask_b32_e64 v109, v109, v110, s[8:9]
	v_mov_b32_e32 v110, v24
	v_mov_b32_e32 v111, v24
	s_nop 1
	v_permlane32_swap_b32_e32 v110, v111
	v_cndmask_b32_e64 v110, v110, v111, s[8:9]
	v_mov_b32_e32 v111, v20
	v_mov_b32_e32 v112, v20
	s_nop 1
	v_permlane32_swap_b32_e32 v111, v112
	v_cndmask_b32_e64 v112, v111, v112, s[8:9]
	v_mov_b32_e32 v111, v25
	v_mov_b32_e32 v113, v25
	s_nop 1
	v_permlane32_swap_b32_e32 v111, v113
	v_cndmask_b32_e64 v111, v111, v113, s[8:9]
	v_mov_b32_e32 v113, v21
	v_mov_b32_e32 v114, v21
	s_nop 1
	v_permlane32_swap_b32_e32 v113, v114
	v_cndmask_b32_e64 v113, v113, v114, s[8:9]
	v_pk_mul_f32 v[114:115], v[24:25], v[96:97]
	v_pk_mul_f32 v[116:117], v[22:23], v[94:95]
	v_pk_mul_f32 v[122:123], v[104:105], v[110:111]
	v_pk_mul_f32 v[126:127], v[102:103], v[106:107]
	v_pk_mul_f32 v[118:119], v[20:21], v[92:93]
	v_pk_mul_f32 v[120:121], v[18:19], v[90:91]
	v_pk_mul_f32 v[124:125], v[100:101], v[112:113]
	v_pk_mul_f32 v[128:129], v[98:99], v[108:109]
	s_and_saveexec_b64 s[40:41], s[10:11]
	s_xor_b64 s[40:41], exec, s[40:41]
	v_pk_add_f32 v[108:109], v[114:115], v[122:123]
	v_pk_add_f32 v[106:107], v[116:117], v[126:127]
	v_pk_add_f32 v[112:113], v[118:119], v[124:125]
	v_pk_add_f32 v[110:111], v[120:121], v[128:129]
	s_andn2_saveexec_b64 s[40:41], s[40:41]
	v_sub_f32_e32 v109, v115, v123
	v_sub_f32_e32 v108, v114, v122
	v_sub_f32_e32 v107, v117, v127
	v_sub_f32_e32 v106, v116, v126
	v_sub_f32_e32 v113, v119, v125
	v_sub_f32_e32 v112, v118, v124
	v_sub_f32_e32 v111, v121, v129
	v_sub_f32_e32 v110, v120, v128
	s_or_b64 exec, exec, s[40:41]

.LBB0_274:
	v_add_u32_e32 v123, 0xa0, v200
	v_cvt_pk_bf16_f32 v86, v86, v87
	v_cvt_pk_bf16_f32 v87, v88, v89
	v_cvt_pk_bf16_f32 v88, v82, v83
	v_lshl_add_u64 v[82:83], v[106:107], 1, s[36:37]
	s_and_b64 vcc, exec, s[14:15]
	v_and_b32_e32 v122, 0xfef, v123
	v_cvt_pk_bf16_f32 v89, v84, v85
	global_store_dwordx4 v[82:83], v[86:89], off
	s_cbranch_vccnz .LBB0_276
	s_waitcnt vmcnt(2)
	v_mov_b64_e32 v[90:91], v[206:207]
	v_mov_b64_e32 v[92:93], v[208:209]
	v_mov_b64_e32 v[94:95], v[210:211]
	v_mov_b64_e32 v[96:97], v[212:213]
	v_mov_b64_e32 v[98:99], v[214:215]
	v_mov_b64_e32 v[100:101], v[216:217]
	v_mov_b64_e32 v[102:103], v[218:219]
	v_mov_b64_e32 v[104:105], v[220:221]
	global_load_dwordx4 v[206:209], v[222:223], off offset:3088
	global_load_dwordx4 v[210:213], v[222:223], off offset:3072
	global_load_dwordx4 v[214:217], v[224:225], off offset:3088
	global_load_dwordx4 v[218:221], v[224:225], off offset:3072
.LBB0_276:
	v_mov_b64_e32 v[84:85], v[16:17]
	v_mov_b64_e32 v[88:89], v[12:13]
	s_and_b64 vcc, exec, s[14:15]
	v_mov_b64_e32 v[82:83], v[14:15]
	v_mov_b64_e32 v[86:87], v[10:11]
	s_cbranch_vccnz .LBB0_282
	v_mov_b32_e32 v82, v14
	v_mov_b32_e32 v83, v14
	s_nop 1
	v_permlane32_swap_b32_e32 v82, v83
	v_cndmask_b32_e64 v82, v82, v83, s[8:9]
	v_mov_b32_e32 v83, v10
	v_mov_b32_e32 v84, v10
	s_nop 1
	v_permlane32_swap_b32_e32 v83, v84
	v_cndmask_b32_e64 v84, v83, v84, s[8:9]
	v_mov_b32_e32 v83, v15
	v_mov_b32_e32 v85, v15
	s_nop 1
	v_permlane32_swap_b32_e32 v83, v85
	v_cndmask_b32_e64 v83, v83, v85, s[8:9]
	v_mov_b32_e32 v85, v11
	v_mov_b32_e32 v86, v11
	s_nop 1
	v_permlane32_swap_b32_e32 v85, v86
	v_cndmask_b32_e64 v85, v85, v86, s[8:9]
	v_mov_b32_e32 v86, v16
	v_mov_b32_e32 v87, v16
	s_nop 1
	v_permlane32_swap_b32_e32 v86, v87
	v_cndmask_b32_e64 v86, v86, v87, s[8:9]
	v_mov_b32_e32 v87, v12
	v_mov_b32_e32 v88, v12
	s_nop 1
	v_permlane32_swap_b32_e32 v87, v88
	v_cndmask_b32_e64 v88, v87, v88, s[8:9]
	v_mov_b32_e32 v87, v17
	v_mov_b32_e32 v89, v17
	s_nop 1
	v_permlane32_swap_b32_e32 v87, v89
	v_cndmask_b32_e64 v87, v87, v89, s[8:9]
	v_mov_b32_e32 v89, v13
	v_mov_b32_e32 v106, v13
	s_nop 1
	v_permlane32_swap_b32_e32 v89, v106
	v_cndmask_b32_e64 v89, v89, v106, s[8:9]
	v_pk_mul_f32 v[106:107], v[16:17], v[96:97]
	v_pk_mul_f32 v[108:109], v[14:15], v[94:95]
	v_pk_mul_f32 v[114:115], v[104:105], v[86:87]
	v_pk_mul_f32 v[118:119], v[102:103], v[82:83]
	v_pk_mul_f32 v[110:111], v[12:13], v[92:93]
	v_pk_mul_f32 v[112:113], v[10:11], v[90:91]
	v_pk_mul_f32 v[116:117], v[100:101], v[88:89]
	v_pk_mul_f32 v[120:121], v[98:99], v[84:85]
	s_and_saveexec_b64 s[40:41], s[10:11]
	s_xor_b64 s[40:41], exec, s[40:41]
	v_pk_add_f32 v[84:85], v[106:107], v[114:115]
	v_pk_add_f32 v[82:83], v[108:109], v[118:119]
	v_pk_add_f32 v[88:89], v[110:111], v[116:117]
	v_pk_add_f32 v[86:87], v[112:113], v[120:121]
	s_andn2_saveexec_b64 s[40:41], s[40:41]
	v_sub_f32_e32 v85, v107, v115
	v_sub_f32_e32 v84, v106, v114
	v_sub_f32_e32 v83, v109, v119
	v_sub_f32_e32 v82, v108, v118
	v_sub_f32_e32 v89, v111, v117
	v_sub_f32_e32 v88, v110, v116
	v_sub_f32_e32 v87, v113, v121
	v_sub_f32_e32 v86, v112, v120
	s_or_b64 exec, exec, s[40:41]

.LBB0_290:
	v_add_u32_e32 v115, 0xb0, v200
	v_cvt_pk_bf16_f32 v78, v78, v79
	v_cvt_pk_bf16_f32 v79, v80, v81
	v_cvt_pk_bf16_f32 v80, v74, v75
	v_lshl_add_u64 v[74:75], v[82:83], 1, s[36:37]
	s_and_b64 vcc, exec, s[14:15]
	v_and_b32_e32 v114, 0xfff, v115
	v_cvt_pk_bf16_f32 v81, v76, v77
	global_store_dwordx4 v[74:75], v[78:81], off
	s_cbranch_vccnz .LBB0_292
	s_waitcnt vmcnt(2)
	v_mov_b64_e32 v[90:91], v[206:207]
	v_mov_b64_e32 v[92:93], v[208:209]
	v_mov_b64_e32 v[94:95], v[210:211]
	v_mov_b64_e32 v[96:97], v[212:213]
	v_mov_b64_e32 v[98:99], v[214:215]
	v_mov_b64_e32 v[100:101], v[216:217]
	v_mov_b64_e32 v[102:103], v[218:219]
	v_mov_b64_e32 v[104:105], v[220:221]
.LBB0_292:
	v_mov_b64_e32 v[76:77], v[8:9]
	v_mov_b64_e32 v[80:81], v[4:5]
	s_and_b64 vcc, exec, s[14:15]
	v_mov_b64_e32 v[74:75], v[6:7]
	v_mov_b64_e32 v[78:79], v[2:3]
	s_cbranch_vccnz .LBB0_298
	v_mov_b32_e32 v74, v6
	v_mov_b32_e32 v75, v6
	s_nop 1
	v_permlane32_swap_b32_e32 v74, v75
	v_cndmask_b32_e64 v74, v74, v75, s[8:9]
	v_mov_b32_e32 v75, v2
	v_mov_b32_e32 v76, v2
	s_nop 1
	v_permlane32_swap_b32_e32 v75, v76
	v_cndmask_b32_e64 v76, v75, v76, s[8:9]
	v_mov_b32_e32 v75, v7
	v_mov_b32_e32 v77, v7
	s_nop 1
	v_permlane32_swap_b32_e32 v75, v77
	v_cndmask_b32_e64 v75, v75, v77, s[8:9]
	v_mov_b32_e32 v77, v3
	v_mov_b32_e32 v78, v3
	s_nop 1
	v_permlane32_swap_b32_e32 v77, v78
	v_cndmask_b32_e64 v77, v77, v78, s[8:9]
	v_mov_b32_e32 v78, v8
	v_mov_b32_e32 v79, v8
	s_nop 1
	v_permlane32_swap_b32_e32 v78, v79
	v_cndmask_b32_e64 v78, v78, v79, s[8:9]
	v_mov_b32_e32 v79, v4
	v_mov_b32_e32 v80, v4
	s_nop 1
	v_permlane32_swap_b32_e32 v79, v80
	v_cndmask_b32_e64 v80, v79, v80, s[8:9]
	v_mov_b32_e32 v79, v9
	v_mov_b32_e32 v81, v9
	s_nop 1
	v_permlane32_swap_b32_e32 v79, v81
	v_cndmask_b32_e64 v79, v79, v81, s[8:9]
	v_mov_b32_e32 v81, v5
	v_mov_b32_e32 v82, v5
	s_nop 1
	v_permlane32_swap_b32_e32 v81, v82
	v_cndmask_b32_e64 v81, v81, v82, s[8:9]
	v_pk_mul_f32 v[82:83], v[8:9], v[96:97]
	v_pk_mul_f32 v[84:85], v[6:7], v[94:95]
	v_pk_mul_f32 v[106:107], v[104:105], v[78:79]
	v_pk_mul_f32 v[110:111], v[102:103], v[74:75]
	v_pk_mul_f32 v[86:87], v[4:5], v[92:93]
	v_pk_mul_f32 v[88:89], v[2:3], v[90:91]
	v_pk_mul_f32 v[108:109], v[100:101], v[80:81]
	v_pk_mul_f32 v[112:113], v[98:99], v[76:77]
	s_and_saveexec_b64 s[40:41], s[10:11]
	s_xor_b64 s[40:41], exec, s[40:41]
	v_pk_add_f32 v[76:77], v[82:83], v[106:107]
	v_pk_add_f32 v[74:75], v[84:85], v[110:111]
	v_pk_add_f32 v[80:81], v[86:87], v[108:109]
	v_pk_add_f32 v[78:79], v[88:89], v[112:113]
	s_andn2_saveexec_b64 s[40:41], s[40:41]
	v_sub_f32_e32 v77, v83, v107
	v_sub_f32_e32 v76, v82, v106
	v_sub_f32_e32 v75, v85, v111
	v_sub_f32_e32 v74, v84, v110
	v_sub_f32_e32 v81, v87, v109
	v_sub_f32_e32 v80, v86, v108
	v_sub_f32_e32 v79, v89, v113
	v_sub_f32_e32 v78, v88, v112
	s_or_b64 exec, exec, s[40:41]
